# cfgN + w_out1 and w_glu weight conversions moved from PRO into the H0-shadow converters
# baseline (speedup 1.0000x reference)
.LBB0_15:
	s_cmp_ge_u32 s99, 2
	s_cbranch_scc1 .Ltr_fwd1
	v_lshlrev_b32_e32 v67, 2, v0
	v_and_b32_e32 v71, 60, v67
	v_bfe_u32 v93, v0, 4, 2
	v_lshlrev_b32_e32 v1, 2, v71
	v_mul_u32_u24_e32 v2, 0x104, v93
	v_add3_u32 v73, v31, v1, v2
	v_lshlrev_b32_e32 v1, 3, v0
	v_and_b32_e32 v2, 56, v1
	v_mul_u32_u24_e32 v3, 0x104, v2
	v_lshlrev_b32_e32 v4, 2, v66
	s_movk_i32 s0, 0x400
	v_mov_b32_e32 v77, 0
	v_add3_u32 v88, v31, v3, v4
	v_or_b32_e32 v89, 32, v66
	v_or_b32_e32 v90, 40, v66
	v_or_b32_e32 v91, 48, v66
	v_or_b32_e32 v92, 56, v66
	v_cmp_gt_i32_e64 s[6:7], s0, v69
	v_lshlrev_b32_e32 v76, 1, v2
	v_lshlrev_b32_e32 v94, 6, v186
	s_cmp_eq_u32 s99, 1
	s_cselect_b64 vcc, s[6:7], 0
	s_and_saveexec_b64 s[0:1], vcc
	s_cbranch_execz .LBB0_50
	v_lshl_add_u64 v[2:3], s[58:59], 0, v[76:77]
	s_mov_b64 s[8:9], 0x3da00000
	v_lshl_add_u64 v[82:83], v[2:3], 0, s[8:9]
	v_lshl_or_b32 v77, s96, 9, v94
	s_lshl_b32 s14, s3, 6
	s_mov_b64 s[8:9], 0
	s_movk_i32 s15, 0x800
	s_movk_i32 s16, 0x3ff
	v_mov_b32_e32 v95, v69
	s_branch .LBB0_18

.LBB0_50:
	s_or_b64 exec, exec, s[0:1]
	s_movk_i32 s0, 0x100
	v_cmp_gt_i32_e32 vcc, s0, v69
	s_cmp_eq_u32 s99, 1
	s_cselect_b64 vcc, vcc, 0
	s_and_saveexec_b64 s[0:1], vcc
	s_cbranch_execz .LBB0_85
	v_mov_b32_e32 v77, 0
	v_lshl_add_u64 v[2:3], s[58:59], 0, v[76:77]
	s_mov_b64 s[8:9], 0x3d800000
	v_lshl_add_u64 v[82:83], v[2:3], 0, s[8:9]
	v_lshl_or_b32 v77, s96, 9, v94
	s_lshl_b32 s14, s3, 6
	s_mov_b64 s[8:9], 0
	s_movk_i32 s15, 0x400
	s_movk_i32 s16, 0xff
	v_mov_b32_e32 v95, v69
	s_branch .LBB0_53
